# attention K/V sharing (2 barriers, lockstep) + removed the now-dead per-wave DMA address arithmetic in the unit loop
# speedup vs baseline: 1.0083x; 1.0083x over previous
.LBB0_431:
	ds_read_b128 v[2:5], v221 offset:32768
	s_cmp_lt_i32 s33, 1
	s_cselect_b64 s[78:79], -1, 0
	s_lshl_b32 s37, s88, 6
	s_waitcnt lgkmcnt(0)
	v_mfma_f32_32x32x16_bf16 v[18:33], v[2:5], v[158:161], 0
	ds_read_b128 v[2:5], v222 offset:32768
	s_waitcnt lgkmcnt(0)
	v_mfma_f32_32x32x16_bf16 v[18:33], v[2:5], v[154:157], v[18:33]
	ds_read_b128 v[2:5], v223 offset:32768
	s_waitcnt lgkmcnt(0)
	v_mfma_f32_32x32x16_bf16 v[18:33], v[2:5], v[150:153], v[18:33]
	ds_read_b128 v[2:5], v224 offset:32768
	s_waitcnt lgkmcnt(0)
	s_waitcnt lgkmcnt(0)
	v_mfma_f32_32x32x16_bf16 v[18:33], v[2:5], v[146:149], v[18:33]
	s_mov_b64 s[4:5], -1
	s_and_b64 vcc, exec, s[78:79]
	s_cbranch_vccz .LBB0_433
	s_nop 0
	s_nop 0
	s_mov_b64 s[4:5], 0
.LBB0_433:
	s_andn2_b64 vcc, exec, s[4:5]
	s_mul_i32 s89, s81, 0x48
	s_cbranch_vccnz .LBB0_435
	s_nop 0
	s_nop 0
.LBB0_435:
	s_mov_b64 s[4:5], -1
	s_and_b64 vcc, exec, s[78:79]
	s_cbranch_vccz .LBB0_437
	s_nop 0
	s_nop 0
	s_nop 0
	s_mov_b64 s[4:5], 0

.LBB0_443:
	ds_read_b128 v[34:37], v222 offset:36864
	ds_read_b128 v[2:5], v221 offset:36864
	s_waitcnt lgkmcnt(0)
	v_mfma_f32_32x32x16_bf16 v[2:17], v[2:5], v[158:161], 0
	v_mfma_f32_32x32x16_bf16 v[2:17], v[34:37], v[154:157], v[2:17]
	ds_read_b128 v[34:37], v223 offset:36864
	s_waitcnt lgkmcnt(0)
	v_mfma_f32_32x32x16_bf16 v[2:17], v[34:37], v[150:153], v[2:17]
	ds_read_b128 v[34:37], v224 offset:36864
	s_waitcnt lgkmcnt(0)
	s_waitcnt lgkmcnt(0)
	v_mfma_f32_32x32x16_bf16 v[2:17], v[34:37], v[146:149], v[2:17]
	v_cndmask_b32_e64 v34, 0, 1, s[78:79]
	v_cmp_ne_u32_e64 s[72:73], 1, v34
	s_andn2_b64 vcc, exec, s[78:79]
	s_mov_b64 s[4:5], -1
	s_cbranch_vccnz .LBB0_445
	s_nop 0
	s_nop 0
	s_mov_b64 s[4:5], 0
.LBB0_445:
	s_andn2_b64 vcc, exec, s[4:5]
	s_mul_i32 s52, s81, 0x60
	s_mul_i32 s51, s81, 0x68
	s_mul_i32 s50, s81, 0x70
	s_mul_i32 s49, s81, 0x78
	s_cbranch_vccnz .LBB0_447
	s_nop 0
	s_nop 0
.LBB0_447:
	s_nop 0
	ds_read_b128 v[34:37], v221 offset:40960
	ds_read_b128 v[52:55], v222 offset:40960
	s_waitcnt lgkmcnt(0)
	v_mfma_f32_32x32x16_bf16 v[34:49], v[34:37], v[158:161], 0
	v_mfma_f32_32x32x16_bf16 v[34:49], v[52:55], v[154:157], v[34:49]
	ds_read_b128 v[52:55], v223 offset:40960
	s_waitcnt lgkmcnt(0)
	v_mfma_f32_32x32x16_bf16 v[34:49], v[52:55], v[150:153], v[34:49]
	ds_read_b128 v[52:55], v224 offset:40960
	s_waitcnt lgkmcnt(0)
	s_waitcnt lgkmcnt(0)
	v_mfma_f32_32x32x16_bf16 v[34:49], v[52:55], v[146:149], v[34:49]
	s_and_b64 vcc, exec, s[72:73]
	s_mov_b64 s[4:5], -1
	s_cbranch_vccnz .LBB0_449
	s_nop 0
	s_nop 0
	s_mov_b64 s[4:5], 0
.LBB0_449:
	s_andn2_b64 vcc, exec, s[4:5]
	s_mul_i32 s46, s81, 0x88
	s_mul_i32 s45, s81, 0x90
	s_mul_i32 s44, s81, 0x98
	s_cbranch_vccnz .LBB0_451
	s_nop 0
	s_nop 0
.LBB0_451:
	s_nop 0
	ds_read_b128 v[50:53], v221 offset:45056
	ds_read_b128 v[66:69], v222 offset:45056
	s_waitcnt lgkmcnt(0)
	v_mfma_f32_32x32x16_bf16 v[50:65], v[50:53], v[158:161], 0
	v_mfma_f32_32x32x16_bf16 v[50:65], v[66:69], v[154:157], v[50:65]
	ds_read_b128 v[66:69], v223 offset:45056
	s_waitcnt lgkmcnt(0)
	v_mfma_f32_32x32x16_bf16 v[50:65], v[66:69], v[150:153], v[50:65]
	ds_read_b128 v[66:69], v224 offset:45056
	s_waitcnt lgkmcnt(0)
	s_waitcnt lgkmcnt(0)
	v_mfma_f32_32x32x16_bf16 v[50:65], v[66:69], v[146:149], v[50:65]
	ds_read_b128 v[66:69], v221 offset:49152
	ds_read_b128 v[82:85], v222 offset:49152
	s_waitcnt lgkmcnt(0)
	v_mfma_f32_32x32x16_bf16 v[66:81], v[66:69], v[158:161], 0
	v_mfma_f32_32x32x16_bf16 v[66:81], v[82:85], v[154:157], v[66:81]
	ds_read_b128 v[82:85], v223 offset:49152
	s_waitcnt lgkmcnt(0)
	v_mfma_f32_32x32x16_bf16 v[66:81], v[82:85], v[150:153], v[66:81]
	ds_read_b128 v[82:85], v224 offset:49152
	s_waitcnt lgkmcnt(0)
	s_waitcnt lgkmcnt(0)
	v_mfma_f32_32x32x16_bf16 v[66:81], v[82:85], v[146:149], v[66:81]
	s_waitcnt vmcnt(0)
	s_barrier
	s_add_i32 s38, s53, 1
	s_cmp_lt_i32 s38, s0
	s_cselect_b64 s[96:97], -1, 0
	s_cmp_ge_i32 s38, s0
	s_mov_b32 s39, s86
	s_mov_b32 s40, s88
	s_mov_b32 s47, s81
	s_mov_b32 s41, s33
	s_mov_b32 s80, s42
	s_mov_b32 s48, s82
	v_mov_b32_e32 v183, v180
	v_mov_b32_e32 v190, v178
	v_mov_b32_e32 v187, v182
	s_cbranch_scc1 .LBB0_466
	v_readlane_b32 s40, v254, 8
	v_readlane_b32 s41, v254, 9
	s_mov_b64 s[4:5], -1
	s_and_b64 vcc, exec, s[40:41]
	s_cbranch_vccz .LBB0_454
	s_mul_i32 s4, s38, s74
	v_readlane_b32 s40, v254, 19
	s_add_i32 s39, s4, s40
	s_mov_b64 s[4:5], 0

.LBB0_459:
	s_lshl_b32 s4, s39, 1
	v_readlane_b32 s5, v254, 14
	s_add_i32 s4, s4, s5
	s_ashr_i32 s39, s4, 11
	s_bfe_u32 s5, s4, 0x70004
	s_lshl_b32 s48, s39, 1
	s_and_b32 s40, s4, 15
	s_lshr_b32 s41, s5, s48
	s_bfm_b32 s4, s48, 0
	s_and_b32 s4, s4, s5
	s_lshl_b32 s5, s41, 7
	s_lshl_b32 s5, s5, s48
	s_or_b32 s80, s5, s4
	v_lshlrev_b32_e32 v82, s48, v192
	v_add_u32_e32 v82, s80, v82
	s_movk_i32 s4, 0xc40
	v_mul_lo_u32 v82, v82, s4
	s_lshl_b32 s47, s40, 6
	v_add_lshl_u32 v84, v82, s47, 1
	s_cmp_lg_u32 s41, 0
	s_cselect_b64 s[4:5], -1, 0
	s_cmp_eq_u32 s41, 0
	v_add_u32_e32 v190, v207, v84
	s_cbranch_scc1 .LBB0_489
	v_mov_b32_e32 v191, v179
	s_cbranch_execnz .LBB0_462
.LBB0_461:
	s_nop 0
	s_nop 0
	s_nop 0
.LBB0_462:
	s_andn2_b64 vcc, exec, s[4:5]
	s_cbranch_vccnz .LBB0_490
	v_mov_b32_e32 v191, v179
	s_nop 0
	s_cbranch_execnz .LBB0_465

.LBB0_471:
	v_max_f32_e32 v33, v18, v18
	v_max_f32_e32 v66, v97, v97
	v_max_f32_e32 v33, v66, v33
	v_max_f32_e32 v66, v20, v20
	v_max_f32_e32 v67, v19, v19
	v_max_f32_e32 v66, v67, v66
	s_mov_b32 s4, 0xff800000
	v_max3_f32 v33, v33, s4, v66
	v_max_f32_e32 v66, v22, v22
	v_max_f32_e32 v67, v21, v21
	v_max_f32_e32 v66, v67, v66
	v_max_f32_e32 v67, v24, v24
	v_max_f32_e32 v68, v23, v23
	v_max_f32_e32 v67, v68, v67
	v_max3_f32 v33, v33, v66, v67
	v_max_f32_e32 v66, v26, v26
	v_max_f32_e32 v67, v25, v25
	v_max_f32_e32 v66, v67, v66
	v_max_f32_e32 v67, v28, v28
	v_max_f32_e32 v68, v27, v27
	v_max_f32_e32 v67, v68, v67
	v_max3_f32 v33, v33, v66, v67
	v_max_f32_e32 v66, v31, v31
	v_max_f32_e32 v67, v29, v29
	v_max_f32_e32 v66, v67, v66
	v_max_f32_e32 v67, v30, v30
	v_max_f32_e32 v68, v32, v32
	v_max_f32_e32 v67, v68, v67
	v_max3_f32 v33, v33, v66, v67
	v_max_f32_e32 v66, v3, v3
	v_max_f32_e32 v67, v2, v2
	v_max_f32_e32 v66, v67, v66
	v_max_f32_e32 v67, v5, v5
	v_max_f32_e32 v68, v4, v4
	v_max_f32_e32 v67, v68, v67
	v_max3_f32 v33, v33, v66, v67
	v_max_f32_e32 v66, v7, v7
	v_max_f32_e32 v67, v6, v6
	v_max_f32_e32 v66, v67, v66
	v_max_f32_e32 v67, v9, v9
	v_max_f32_e32 v68, v8, v8
	v_max_f32_e32 v67, v68, v67
	v_max3_f32 v33, v33, v66, v67
	v_max_f32_e32 v66, v11, v11
	v_max_f32_e32 v67, v10, v10
	v_max_f32_e32 v66, v67, v66
	v_max_f32_e32 v67, v13, v13
	v_max_f32_e32 v68, v12, v12
	v_max_f32_e32 v67, v68, v67
	v_max3_f32 v33, v33, v66, v67
	v_max_f32_e32 v66, v15, v15
	v_max_f32_e32 v67, v14, v14
	v_max_f32_e32 v66, v67, v66
	v_max_f32_e32 v67, v17, v17
	v_max_f32_e32 v68, v16, v16
	v_max_f32_e32 v67, v68, v67
	v_max3_f32 v33, v33, v66, v67
	v_max_f32_e32 v66, v35, v35
	v_max_f32_e32 v67, v34, v34
	v_max_f32_e32 v66, v67, v66
	v_max_f32_e32 v67, v37, v37
	v_max_f32_e32 v68, v36, v36
	v_max_f32_e32 v67, v68, v67
	v_max3_f32 v33, v33, v66, v67
	v_max_f32_e32 v66, v39, v39
	v_max_f32_e32 v67, v38, v38
	v_max_f32_e32 v66, v67, v66
	v_max_f32_e32 v67, v41, v41
	v_max_f32_e32 v68, v40, v40
	v_max_f32_e32 v67, v68, v67
	v_max3_f32 v33, v33, v66, v67
	v_max_f32_e32 v66, v43, v43
	v_max_f32_e32 v67, v42, v42
	v_max_f32_e32 v66, v67, v66
	v_max_f32_e32 v67, v45, v45
	v_max_f32_e32 v68, v44, v44
	v_max_f32_e32 v67, v68, v67
	v_max3_f32 v33, v33, v66, v67
	v_max_f32_e32 v66, v47, v47
	v_max_f32_e32 v67, v46, v46
	v_max_f32_e32 v66, v67, v66
	v_max_f32_e32 v67, v49, v49
	v_max_f32_e32 v68, v48, v48
	v_max_f32_e32 v67, v68, v67
	v_max3_f32 v33, v33, v66, v67
	v_max_f32_e32 v66, v51, v51
	v_max_f32_e32 v67, v50, v50
	v_max_f32_e32 v66, v67, v66
	v_max_f32_e32 v67, v53, v53
	v_max_f32_e32 v68, v52, v52
	v_max_f32_e32 v67, v68, v67
	v_max3_f32 v33, v33, v66, v67
	v_max_f32_e32 v66, v55, v55
	v_max_f32_e32 v67, v54, v54
	v_max_f32_e32 v66, v67, v66
	v_max_f32_e32 v67, v57, v57
	v_max_f32_e32 v68, v56, v56
	v_max_f32_e32 v67, v68, v67
	v_max3_f32 v33, v33, v66, v67
	v_max_f32_e32 v66, v59, v59
	v_max_f32_e32 v67, v58, v58
	v_max_f32_e32 v66, v67, v66
	v_max_f32_e32 v67, v61, v61
	v_max_f32_e32 v68, v60, v60
	v_max_f32_e32 v67, v68, v67
	v_max3_f32 v33, v33, v66, v67
	v_max_f32_e32 v66, v63, v63
	v_max_f32_e32 v67, v62, v62
	v_max_f32_e32 v66, v67, v66
	v_max_f32_e32 v67, v65, v65
	v_max_f32_e32 v68, v64, v64
	v_max_f32_e32 v67, v68, v67
	v_max3_f32 v33, v33, v66, v67
	v_max_f32_e32 v66, v83, v83
	v_max_f32_e32 v67, v82, v82
	v_max_f32_e32 v66, v67, v66
	v_max_f32_e32 v67, v85, v85
	v_max_f32_e32 v68, v84, v84
	v_max_f32_e32 v67, v68, v67
	v_max3_f32 v33, v33, v66, v67
	v_max_f32_e32 v66, v87, v87
	v_max_f32_e32 v67, v86, v86
	v_max_f32_e32 v66, v67, v66
	v_max_f32_e32 v67, v89, v89
	v_max_f32_e32 v68, v88, v88
	v_max_f32_e32 v67, v68, v67
	v_max3_f32 v33, v33, v66, v67
	v_max_f32_e32 v66, v91, v91
	v_max_f32_e32 v67, v90, v90
	v_max_f32_e32 v66, v67, v66
	v_max_f32_e32 v67, v93, v93
	v_max_f32_e32 v68, v92, v92
	v_max_f32_e32 v67, v68, v67
	v_cndmask_b32_e64 v70, v81, v226, s[78:79]
	v_max3_f32 v33, v33, v66, v67
	v_max_f32_e32 v66, v95, v95
	v_max_f32_e32 v67, v94, v94
	v_max_f32_e32 v66, v67, v66
	v_max_f32_e32 v67, v70, v70
	v_max_f32_e32 v68, v96, v96
	v_max_f32_e32 v67, v68, v67
	v_max3_f32 v33, v33, v66, v67
	v_and_b32_e32 v67, 64, v209
	v_xor_b32_e32 v66, 32, v209
	v_add_u32_e32 v67, 64, v67
	v_cmp_lt_i32_e32 vcc, v66, v67
	s_nop 1
	v_cndmask_b32_e32 v66, v209, v66, vcc
	v_lshlrev_b32_e32 v118, 2, v66
	ds_bpermute_b32 v66, v118, v33
	s_waitcnt lgkmcnt(0)
	v_max_f32_e32 v66, v66, v66
	v_max_f32_e32 v66, v33, v66
	v_sub_f32_e32 v33, v97, v66
	v_exp_f32_e32 v33, v33
	v_sub_f32_e32 v18, v18, v66
	v_exp_f32_e32 v18, v18
	v_sub_f32_e32 v19, v19, v66
	v_exp_f32_e32 v19, v19
	v_sub_f32_e32 v20, v20, v66
	v_exp_f32_e32 v20, v20
	v_sub_f32_e32 v21, v21, v66
	v_add_f32_e32 v67, 0, v33
	v_exp_f32_e32 v21, v21
	v_sub_f32_e32 v22, v22, v66
	v_add_f32_e32 v67, v18, v67
	v_exp_f32_e32 v22, v22
	v_sub_f32_e32 v23, v23, v66
	v_add_f32_e32 v67, v19, v67
	v_exp_f32_e32 v23, v23
	v_sub_f32_e32 v24, v24, v66
	v_add_f32_e32 v67, v20, v67
	v_exp_f32_e32 v24, v24
	v_sub_f32_e32 v25, v25, v66
	v_add_f32_e32 v67, v21, v67
	v_exp_f32_e32 v119, v25
	v_sub_f32_e32 v25, v26, v66
	v_add_f32_e32 v67, v22, v67
	v_exp_f32_e32 v120, v25
	v_sub_f32_e32 v25, v27, v66
	v_add_f32_e32 v67, v23, v67
	v_exp_f32_e32 v121, v25
	v_sub_f32_e32 v26, v28, v66
	v_add_f32_e32 v25, v24, v67
	v_exp_f32_e32 v122, v26
	v_sub_f32_e32 v26, v29, v66
	v_add_f32_e32 v25, v119, v25
	v_exp_f32_e32 v123, v26
	v_sub_f32_e32 v26, v31, v66
	v_add_f32_e32 v25, v120, v25
	v_exp_f32_e32 v124, v26
	v_sub_f32_e32 v26, v32, v66
	v_add_f32_e32 v25, v121, v25
	v_exp_f32_e32 v125, v26
	v_sub_f32_e32 v26, v30, v66
	v_add_f32_e32 v25, v122, v25
	v_exp_f32_e32 v126, v26
	v_sub_f32_e32 v2, v2, v66
	v_add_f32_e32 v25, v123, v25
	v_exp_f32_e32 v103, v2
	v_sub_f32_e32 v2, v3, v66
	v_add_f32_e32 v25, v124, v25
	v_exp_f32_e32 v106, v2
	v_sub_f32_e32 v2, v4, v66
	v_add_f32_e32 v25, v125, v25
	v_exp_f32_e32 v107, v2
	v_sub_f32_e32 v3, v5, v66
	v_add_f32_e32 v2, v126, v25
	v_exp_f32_e32 v110, v3
	v_sub_f32_e32 v3, v6, v66
	v_add_f32_e32 v2, v103, v2
	v_exp_f32_e32 v111, v3
	v_sub_f32_e32 v3, v7, v66
	v_add_f32_e32 v2, v106, v2
	v_exp_f32_e32 v114, v3
	v_sub_f32_e32 v3, v8, v66
	v_add_f32_e32 v2, v107, v2
	v_exp_f32_e32 v115, v3
	v_sub_f32_e32 v3, v9, v66
	v_add_f32_e32 v2, v110, v2
	v_exp_f32_e32 v117, v3
	v_sub_f32_e32 v3, v10, v66
	v_add_f32_e32 v2, v111, v2
	v_exp_f32_e32 v102, v3
	v_sub_f32_e32 v3, v11, v66
	v_add_f32_e32 v2, v114, v2
	v_exp_f32_e32 v104, v3
	v_sub_f32_e32 v3, v12, v66
	v_add_f32_e32 v2, v115, v2
	v_exp_f32_e32 v105, v3
	v_sub_f32_e32 v3, v13, v66
	v_add_f32_e32 v2, v117, v2
	v_exp_f32_e32 v108, v3
	v_sub_f32_e32 v3, v14, v66
	v_add_f32_e32 v2, v102, v2
	v_exp_f32_e32 v109, v3
	v_sub_f32_e32 v3, v15, v66
	v_add_f32_e32 v2, v104, v2
	v_exp_f32_e32 v112, v3
	v_sub_f32_e32 v3, v16, v66
	v_add_f32_e32 v2, v105, v2
	v_exp_f32_e32 v113, v3
	v_sub_f32_e32 v3, v17, v66
	v_add_f32_e32 v2, v108, v2
	v_exp_f32_e32 v116, v3
	v_sub_f32_e32 v3, v34, v66
	v_add_f32_e32 v2, v109, v2
	v_exp_f32_e32 v72, v3
	v_sub_f32_e32 v3, v35, v66
	v_add_f32_e32 v2, v112, v2
	v_exp_f32_e32 v75, v3
	v_sub_f32_e32 v3, v36, v66
	v_add_f32_e32 v2, v113, v2
	v_exp_f32_e32 v76, v3
	v_sub_f32_e32 v3, v37, v66
	v_add_f32_e32 v2, v116, v2
	v_exp_f32_e32 v79, v3
	v_sub_f32_e32 v3, v38, v66
	v_add_f32_e32 v2, v72, v2
	v_exp_f32_e32 v80, v3
	v_sub_f32_e32 v3, v39, v66
	v_add_f32_e32 v2, v75, v2
	v_exp_f32_e32 v98, v3
	v_sub_f32_e32 v3, v40, v66
	v_add_f32_e32 v2, v76, v2
	v_exp_f32_e32 v99, v3
	v_sub_f32_e32 v3, v41, v66
	v_add_f32_e32 v2, v79, v2
	v_exp_f32_e32 v101, v3
	v_sub_f32_e32 v3, v42, v66
	v_add_f32_e32 v2, v80, v2
	v_exp_f32_e32 v71, v3
	v_sub_f32_e32 v3, v43, v66
	v_add_f32_e32 v2, v98, v2
	v_exp_f32_e32 v73, v3
	v_sub_f32_e32 v3, v44, v66
	v_add_f32_e32 v2, v99, v2
	v_exp_f32_e32 v74, v3
	v_sub_f32_e32 v3, v45, v66
	v_add_f32_e32 v2, v101, v2
	v_exp_f32_e32 v77, v3
	v_sub_f32_e32 v3, v46, v66
	v_add_f32_e32 v2, v71, v2
	v_exp_f32_e32 v78, v3
	v_sub_f32_e32 v3, v47, v66
	v_add_f32_e32 v2, v73, v2
	v_exp_f32_e32 v81, v3
	v_sub_f32_e32 v3, v48, v66
	v_add_f32_e32 v2, v74, v2
	v_exp_f32_e32 v97, v3
	v_sub_f32_e32 v3, v49, v66
	v_add_f32_e32 v2, v77, v2
	v_exp_f32_e32 v100, v3
	v_sub_f32_e32 v3, v50, v66
	v_add_f32_e32 v2, v78, v2
	v_exp_f32_e32 v41, v3
	v_sub_f32_e32 v3, v51, v66
	v_add_f32_e32 v2, v81, v2
	v_exp_f32_e32 v46, v3
	v_sub_f32_e32 v3, v52, v66
	v_add_f32_e32 v2, v97, v2
	v_exp_f32_e32 v47, v3
	v_sub_f32_e32 v3, v53, v66
	v_add_f32_e32 v2, v100, v2
	v_exp_f32_e32 v53, v3
	v_sub_f32_e32 v3, v54, v66
	v_add_f32_e32 v2, v41, v2
	v_exp_f32_e32 v54, v3
	v_sub_f32_e32 v3, v55, v66
	v_add_f32_e32 v2, v46, v2
	v_exp_f32_e32 v67, v3
	v_sub_f32_e32 v3, v56, v66
	v_add_f32_e32 v2, v47, v2
	v_exp_f32_e32 v68, v3
	v_sub_f32_e32 v3, v57, v66
	v_add_f32_e32 v2, v53, v2
	v_exp_f32_e32 v69, v3
	v_sub_f32_e32 v3, v58, v66
	v_add_f32_e32 v2, v54, v2
	v_exp_f32_e32 v38, v3
	v_sub_f32_e32 v3, v59, v66
	v_add_f32_e32 v2, v67, v2
	v_exp_f32_e32 v44, v3
	v_sub_f32_e32 v3, v60, v66
	v_add_f32_e32 v2, v68, v2
	v_exp_f32_e32 v45, v3
	v_sub_f32_e32 v3, v61, v66
	v_add_f32_e32 v2, v69, v2
	v_exp_f32_e32 v51, v3
	v_sub_f32_e32 v3, v62, v66
	v_add_f32_e32 v2, v38, v2
	v_exp_f32_e32 v52, v3
	v_sub_f32_e32 v3, v63, v66
	v_add_f32_e32 v2, v44, v2
	v_exp_f32_e32 v57, v3
	v_sub_f32_e32 v3, v64, v66
	v_add_f32_e32 v2, v45, v2
	v_exp_f32_e32 v58, v3
	v_sub_f32_e32 v3, v65, v66
	v_add_f32_e32 v2, v51, v2
	v_exp_f32_e32 v62, v3
	v_sub_f32_e32 v3, v82, v66
	v_add_f32_e32 v2, v52, v2
	v_exp_f32_e32 v37, v3
	v_sub_f32_e32 v3, v83, v66
	v_add_f32_e32 v2, v57, v2
	v_exp_f32_e32 v42, v3
	v_sub_f32_e32 v3, v84, v66
	v_add_f32_e32 v2, v58, v2
	v_exp_f32_e32 v43, v3
	v_sub_f32_e32 v3, v85, v66
	v_add_f32_e32 v2, v62, v2
	v_exp_f32_e32 v49, v3
	v_sub_f32_e32 v3, v86, v66
	v_add_f32_e32 v2, v37, v2
	v_exp_f32_e32 v50, v3
	v_sub_f32_e32 v3, v87, v66
	v_add_f32_e32 v2, v42, v2
	v_exp_f32_e32 v55, v3
	v_sub_f32_e32 v3, v88, v66
	v_add_f32_e32 v2, v43, v2
	v_exp_f32_e32 v56, v3
	v_sub_f32_e32 v3, v89, v66
	v_add_f32_e32 v2, v49, v2
	v_exp_f32_e32 v61, v3
	v_sub_f32_e32 v3, v90, v66
	v_add_f32_e32 v2, v50, v2
	v_exp_f32_e32 v36, v3
	v_sub_f32_e32 v3, v91, v66
	v_add_f32_e32 v2, v55, v2
	v_exp_f32_e32 v39, v3
	v_sub_f32_e32 v3, v92, v66
	v_add_f32_e32 v2, v56, v2
	v_exp_f32_e32 v40, v3
	v_add_f32_e32 v2, v61, v2
	v_add_f32_e32 v2, v36, v2
	v_add_f32_e32 v2, v39, v2
	v_add_f32_e32 v14, v40, v2
	v_sub_f32_e32 v2, v93, v66
	v_exp_f32_e32 v48, v2
	v_cvt_pk_bf16_f32 v2, v33, v18
	v_cvt_pk_bf16_f32 v3, v19, v20
	v_cvt_pk_bf16_f32 v4, v21, v22
	v_cvt_pk_bf16_f32 v5, v23, v24
	ds_read_b64_tr_b16 v[10:11], v195
	ds_read_b64_tr_b16 v[12:13], v195 offset:1024
	ds_read_b64_tr_b16 v[6:7], v196
	ds_read_b64_tr_b16 v[8:9], v196 offset:1024
	s_waitcnt lgkmcnt(0)
	s_nop 0
	v_add_f32_e32 v34, v48, v14
	v_mfma_f32_32x32x16_bf16 v[18:33], v[10:13], v[2:5], 0
	v_sub_f32_e32 v10, v94, v66
	v_exp_f32_e32 v63, v10
	v_sub_f32_e32 v10, v95, v66
	v_exp_f32_e32 v65, v10
	v_sub_f32_e32 v10, v96, v66
	v_exp_f32_e32 v64, v10
	v_sub_f32_e32 v35, v70, v66
	v_mfma_f32_32x32x16_bf16 v[2:17], v[6:9], v[2:5], 0
	v_exp_f32_e32 v70, v35
	v_add_f32_e32 v34, v63, v34
	v_cvt_pk_bf16_f32 v82, v119, v120
	v_cvt_pk_bf16_f32 v83, v121, v122
	v_cvt_pk_bf16_f32 v84, v123, v124
	v_cvt_pk_bf16_f32 v85, v125, v126
	ds_read_b64_tr_b16 v[90:91], v197
	ds_read_b64_tr_b16 v[92:93], v197 offset:1024
	ds_read_b64_tr_b16 v[86:87], v198
	ds_read_b64_tr_b16 v[88:89], v198 offset:1024
	s_waitcnt lgkmcnt(0)
	v_add_f32_e32 v34, v65, v34
	v_mfma_f32_32x32x16_bf16 v[18:33], v[90:93], v[82:85], v[18:33]
	v_add_f32_e32 v34, v64, v34
	v_add_f32_e32 v59, v70, v34
	ds_bpermute_b32 v60, v118, v59
	v_mfma_f32_32x32x16_bf16 v[2:17], v[86:89], v[82:85], v[2:17]
	s_and_b64 vcc, exec, s[72:73]
	s_mov_b64 s[4:5], -1
	s_cbranch_vccnz .LBB0_473
	s_lshl_b32 s90, s37, 1
	s_nop 0
	s_add_i32 m0, s75, 0x800
	s_nop 0
	s_mov_b64 s[4:5], 0
.LBB0_473:
	s_andn2_b64 vcc, exec, s[4:5]
	s_cbranch_vccnz .LBB0_475
	s_lshl_b32 s4, s81, 6
	s_nop 0
	s_add_i32 m0, s75, 0x800
	s_nop 0
.LBB0_475:
	s_nop 0
	v_cvt_pk_bf16_f32 v82, v103, v106
	v_cvt_pk_bf16_f32 v83, v107, v110
	v_cvt_pk_bf16_f32 v84, v111, v114
	v_cvt_pk_bf16_f32 v85, v115, v117
	ds_read_b64_tr_b16 v[90:91], v199
	ds_read_b64_tr_b16 v[92:93], v199 offset:1024
	ds_read_b64_tr_b16 v[86:87], v200
	ds_read_b64_tr_b16 v[88:89], v200 offset:1024
	s_waitcnt lgkmcnt(0)
	s_nop 0
	v_mfma_f32_32x32x16_bf16 v[18:33], v[90:93], v[82:85], v[18:33]
	v_mfma_f32_32x32x16_bf16 v[2:17], v[86:89], v[82:85], v[2:17]
	v_cvt_pk_bf16_f32 v82, v102, v104
	v_cvt_pk_bf16_f32 v83, v105, v108
	v_cvt_pk_bf16_f32 v84, v109, v112
	v_cvt_pk_bf16_f32 v85, v113, v116
	ds_read_b64_tr_b16 v[90:91], v201
	ds_read_b64_tr_b16 v[92:93], v201 offset:1024
	ds_read_b64_tr_b16 v[86:87], v202
	ds_read_b64_tr_b16 v[88:89], v202 offset:1024
	s_waitcnt lgkmcnt(0)
	s_nop 0
	v_mfma_f32_32x32x16_bf16 v[18:33], v[90:93], v[82:85], v[18:33]
	v_mfma_f32_32x32x16_bf16 v[2:17], v[86:89], v[82:85], v[2:17]
	s_and_b64 vcc, exec, s[72:73]
	s_mov_b64 s[4:5], -1
	s_cbranch_vccnz .LBB0_477
	s_lshl_b32 s90, s37, 1
	s_nop 0
	s_nop 0
	s_mov_b64 s[4:5], 0
.LBB0_477:
	s_andn2_b64 vcc, exec, s[4:5]
	s_cbranch_vccnz .LBB0_479
	s_nop 0
	s_nop 0
.LBB0_479:
	s_nop 0
	v_cvt_pk_bf16_f32 v82, v72, v75
	v_cvt_pk_bf16_f32 v83, v76, v79
	v_cvt_pk_bf16_f32 v84, v80, v98
	v_cvt_pk_bf16_f32 v85, v99, v101
	ds_read_b64_tr_b16 v[90:91], v195 offset:8192
	ds_read_b64_tr_b16 v[92:93], v195 offset:9216
	ds_read_b64_tr_b16 v[86:87], v196 offset:8192
	ds_read_b64_tr_b16 v[88:89], v196 offset:9216
	s_waitcnt lgkmcnt(0)
	v_cvt_pk_bf16_f32 v72, v71, v73
	v_cvt_pk_bf16_f32 v73, v74, v77
	v_cvt_pk_bf16_f32 v74, v78, v81
	v_cvt_pk_bf16_f32 v75, v97, v100
	s_nop 0
	v_mfma_f32_32x32x16_bf16 v[18:33], v[90:93], v[82:85], v[18:33]
	v_mfma_f32_32x32x16_bf16 v[2:17], v[86:89], v[82:85], v[2:17]
	ds_read_b64_tr_b16 v[80:81], v197 offset:8192
	ds_read_b64_tr_b16 v[82:83], v197 offset:9216
	ds_read_b64_tr_b16 v[76:77], v198 offset:8192
	ds_read_b64_tr_b16 v[78:79], v198 offset:9216
	s_waitcnt lgkmcnt(0)
	s_nop 0
	v_mfma_f32_32x32x16_bf16 v[18:33], v[80:83], v[72:75], v[18:33]
	v_mfma_f32_32x32x16_bf16 v[2:17], v[76:79], v[72:75], v[2:17]
	s_and_b64 vcc, exec, s[72:73]
	s_mov_b64 s[4:5], -1
	s_cbranch_vccnz .LBB0_481
	v_mov_b32_e32 v71, v0
	s_lshl_b32 s90, s37, 1
	v_bfe_u32 v76, v71, 3, 3
	s_add_i32 m0, s75, 0x800
	v_or_b32_e32 v71, s20, v76
	v_mul_lo_u32 v71, v71, s81
	v_add_u32_e32 v71, s82, v71
	v_max_i32_e32 v71, 0, v71
	s_mov_b64 s[4:5], 0
.LBB0_481:
	s_andn2_b64 vcc, exec, s[4:5]
	s_cbranch_vccnz .LBB0_483
	s_lshl_b32 s4, s81, 7
	s_nop 0
	s_add_i32 m0, s75, 0x800
	s_nop 0
